# lambda-parameter loads issued before the post-pooling drain+barrier (plus P6 straight-line scatter and attention prologue overlap)
# baseline (speedup 1.0000x reference)
.LBB0_317:
	s_load_dwordx8 s[4:11], s[34:35], 0x38
	v_lshlrev_b32_e32 v1, 2, v254
	s_waitcnt lgkmcnt(0)
	global_load_dword v2, v1, s[4:5]
	global_load_dword v3, v1, s[6:7]
	global_load_dword v4, v1, s[8:9]
	global_load_dword v5, v1, s[10:11]
	s_waitcnt vmcnt(0)
	s_barrier
	v_mbcnt_lo_u32_b32 v1, -1, 0
	v_mbcnt_hi_u32_b32 v1, -1, v1
	v_and_b32_e32 v6, 64, v1
	v_xor_b32_e32 v7, 1, v1
	v_add_u32_e32 v6, 64, v6
	v_cmp_lt_i32_e32 vcc, v7, v6
	v_xor_b32_e32 v8, 2, v1
	v_xor_b32_e32 v9, 4, v1
	v_cndmask_b32_e32 v7, v1, v7, vcc
	v_lshlrev_b32_e32 v7, 2, v7
	v_cmp_lt_i32_e32 vcc, v8, v6
	v_xor_b32_e32 v10, 8, v1
	v_xor_b32_e32 v11, 16, v1
	v_cndmask_b32_e32 v8, v1, v8, vcc
	v_lshlrev_b32_e32 v8, 2, v8
	v_cmp_lt_i32_e32 vcc, v9, v6
	v_xor_b32_e32 v12, 32, v1
	s_mov_b32 s73, 4
	s_waitcnt vmcnt(2)
	v_mul_f32_e32 v13, v2, v3
	ds_bpermute_b32 v13, v7, v13
	s_waitcnt vmcnt(0)
	v_mul_f32_e32 v14, v4, v5
	ds_bpermute_b32 v7, v7, v14
	s_waitcnt lgkmcnt(1)
	v_fmac_f32_e32 v13, v2, v3
	ds_bpermute_b32 v2, v8, v13
	s_waitcnt lgkmcnt(1)
	v_fmac_f32_e32 v7, v4, v5
	ds_bpermute_b32 v3, v8, v7
	v_cndmask_b32_e32 v4, v1, v9, vcc
	v_lshlrev_b32_e32 v4, 2, v4
	s_waitcnt lgkmcnt(1)
	v_add_f32_e32 v2, v13, v2
	ds_bpermute_b32 v5, v4, v2
	s_waitcnt lgkmcnt(1)
	v_add_f32_e32 v3, v7, v3
	ds_bpermute_b32 v4, v4, v3
	v_cmp_lt_i32_e32 vcc, v10, v6
	s_waitcnt lgkmcnt(1)
	v_add_f32_e32 v2, v2, v5
	v_cndmask_b32_e32 v7, v1, v10, vcc
	v_lshlrev_b32_e32 v7, 2, v7
	s_waitcnt lgkmcnt(0)
	v_add_f32_e32 v3, v3, v4
	ds_bpermute_b32 v4, v7, v2
	ds_bpermute_b32 v5, v7, v3
	v_cmp_lt_i32_e32 vcc, v11, v6
	s_waitcnt lgkmcnt(1)
	v_add_f32_e32 v2, v2, v4
	v_cndmask_b32_e32 v7, v1, v11, vcc
	v_lshlrev_b32_e32 v7, 2, v7
	s_waitcnt lgkmcnt(0)
	v_add_f32_e32 v4, v3, v5
	ds_bpermute_b32 v3, v7, v2
	ds_bpermute_b32 v5, v7, v4
	v_cmp_lt_i32_e32 vcc, v12, v6
	s_waitcnt lgkmcnt(1)
	v_add_f32_e32 v3, v2, v3
	v_cndmask_b32_e32 v1, v1, v12, vcc
	v_lshlrev_b32_e32 v1, 2, v1
	s_waitcnt lgkmcnt(0)
	v_add_f32_e32 v2, v4, v5
	ds_bpermute_b32 v5, v1, v3
	ds_bpermute_b32 v4, v1, v2
	v_cmp_eq_u32_e32 vcc, 0, v219
	s_and_saveexec_b64 s[4:5], vcc
	s_cbranch_execz .LBB0_319
	s_waitcnt lgkmcnt(1)
	v_add_f32_e32 v3, v3, v5
	s_waitcnt lgkmcnt(0)
	v_add_f32_e32 v2, v2, v4
	v_mul_f32_e32 v3, 0x3fb8aa3b, v3
	v_mul_f32_e32 v2, 0x3fb8aa3b, v2
	v_exp_f32_e32 v3, v3
	v_exp_f32_e32 v2, v2
	s_add_i32 s0, 0, 0x203f0
	v_sub_f32_e32 v2, v3, v2
	v_add_f32_e32 v2, 0x3e4ccccd, v2
	v_mov_b32_e32 v3, s0
	ds_write_b32 v3, v2
